# v36: v25 + attention window search: wave max by DPP + readlane instead of six ds_bpermute round trips per search step
# baseline (speedup 1.0000x reference)
; __device__ __forceinline__ void fox_phase(const Frame& F, char* lds, int& sg_first, int& sg_count) {
;     ...
;                 for (int t = Wc + F.tid; t < SEQ; t += NTHREADS) mx = fmaxf(mx, bl[t - Wc] - bl[t]);
; #pragma unroll
;                 for (int o = 1; o < 64; o <<= 1) mx = fmaxf(mx, __shfl_xor(mx, o));
;                 __syncthreads(); if (F.lane == 0) red[F.wave] = mx; __syncthreads();
;                 float m8 = red[0];
; #pragma unroll
;                 for (int i = 1; i < 8; ++i) m8 = fmaxf(m8, red[i]);
.LBB0_463:
	s_or_b64 exec, exec, s[6:7]
	v_max_f32_e32 v2, v3, v3
	s_waitcnt lgkmcnt(0)
	s_barrier
	s_nop 0
	v_max_f32_dpp v2, v2, v2 quad_perm:[1,0,3,2] row_mask:0xf bank_mask:0xf
	s_nop 1
	v_max_f32_dpp v2, v2, v2 quad_perm:[2,3,0,1] row_mask:0xf bank_mask:0xf
	s_nop 1
	v_max_f32_dpp v2, v2, v2 row_half_mirror row_mask:0xf bank_mask:0xf
	s_nop 1
	v_max_f32_dpp v2, v2, v2 row_mirror row_mask:0xf bank_mask:0xf
	s_nop 1
	v_readlane_b32 s0, v2, 0
	v_readlane_b32 s1, v2, 16
	v_readlane_b32 s2, v2, 32
	v_readlane_b32 s3, v2, 48
	s_nop 1
	v_mov_b32_e32 v2, s0
	v_max_f32_e32 v2, s1, v2
	v_max_f32_e32 v2, s2, v2
	v_max_f32_e32 v2, s3, v2
	s_and_saveexec_b64 s[0:1], vcc
	s_cbranch_execz .LBB0_452
	v_mov_b32_e32 v3, s23
	ds_write_b32 v3, v2
	s_branch .LBB0_452
